# down and out GEMM epilogues issue the second batch's 8 residual loads together with the first batch's (one exposed load latency per unit instead of two); snake MFMA order
# baseline (speedup 1.0000x reference)
; __device__ __forceinline__ unsigned cvt_pk_bf16(float lo, float hi) { f32x2_c v = {lo, hi}; bf16x2_c b = __builtin_convertvector(v, bf16x2_c); return __builtin_bit_cast(unsigned, b); }
; __device__ __forceinline__ float bf_lo(unsigned u) { return __uint_as_float(u << 16); }
; __device__ __forceinline__ float bf_hi(unsigned u) { return __uint_as_float(u & 0xffff0000u); }
;     __device__ __forceinline__ void operator()(const f32x4 (&acc)[2][2][4][2], const Unit& u, int wr, int wc, int fr, int fq) const {
;     ...
;         for (int ai = 0; ai < 2; ++ai) {
;             u32x4 xv[4][2];
; #pragma unroll
;             for (int m = 0; m < 4; ++m)
; #pragma unroll
;                 for (int bj = 0; bj < 2; ++bj) xv[m][bj] = *(const u32x4*)(Hx + (size_t)(row0 + ai * HALF + m * 16) * LDT + col0 + bj * HALF);
;             float ssm[4];
; #pragma unroll
;             for (int m = 0; m < 4; ++m) { const int row = row0 + ai * HALF + m * 16; bf16_t* hp = Hx + (size_t)row * LDT + col0;
;                 float ss = 0.f;
; #pragma unroll
;                 for (int bj = 0; bj < 2; ++bj) { const u32x4 x = xv[m][bj]; const f32x4 a0 = acc[ai][bj][m][0], a1 = acc[ai][bj][m][1];
;                     const float y0 = bf_lo(x.x) + a0[0] * scale, y1 = bf_hi(x.x) + a0[1] * scale, y2 = bf_lo(x.y) + a0[2] * scale, y3 = bf_hi(x.y) + a0[3] * scale;
;                     const float y4 = bf_lo(x.z) + a1[0] * scale, y5 = bf_hi(x.z) + a1[1] * scale, y6 = bf_lo(x.w) + a1[2] * scale, y7 = bf_hi(x.w) + a1[3] * scale;
;                     ss += ((y0 * y0 + y1 * y1) + (y2 * y2 + y3 * y3)) + ((y4 * y4 + y5 * y5) + (y6 * y6 + y7 * y7));
;                     u32x4 w; w.x = cvt_pk_bf16(y0, y1); w.y = cvt_pk_bf16(y2, y3); w.z = cvt_pk_bf16(y4, y5); w.w = cvt_pk_bf16(y6, y7);
;                     *(u32x4*)(hp + bj * HALF) = w; }
.LBB0_236:
	v_lshl_or_b32 v116, s2, 8, v177
	v_ashrrev_i32_e32 v117, 31, v116
	v_readlane_b32 s24, v254, 23
	v_lshlrev_b64 v[166:167], 1, v[116:117]
	v_readlane_b32 s25, v254, 24
	v_lshl_add_u32 v181, s3, 8, v174
	v_or_b32_e32 v196, 16, v181
	v_lshl_add_u64 v[168:169], s[24:25], 0, v[166:167]
	v_mad_i64_i32 v[116:117], s[4:5], v181, s81, v[168:169]
	global_load_dwordx4 v[182:185], v[116:117], off
	global_load_dwordx4 v[156:159], v[116:117], off offset:256
	v_mad_i64_i32 v[116:117], s[4:5], v196, s81, v[168:169]
	global_load_dwordx4 v[152:155], v[116:117], off
	global_load_dwordx4 v[148:151], v[116:117], off offset:256
	v_or_b32_e32 v195, 32, v181
	v_mad_i64_i32 v[116:117], s[4:5], v195, s81, v[168:169]
	global_load_dwordx4 v[144:147], v[116:117], off
	global_load_dwordx4 v[132:135], v[116:117], off offset:256
	v_and_b32_e32 v119, 64, v210
	v_xor_b32_e32 v118, 16, v210
	v_add_u32_e32 v119, 64, v119
	v_cmp_lt_i32_e32 vcc, v118, v119
	v_or_b32_e32 v194, 48, v181
	v_mad_i64_i32 v[116:117], s[4:5], v194, s81, v[168:169]
	v_cndmask_b32_e32 v118, v210, v118, vcc
	v_lshlrev_b32_e32 v180, 2, v118
	v_xor_b32_e32 v118, 32, v210
	v_cmp_lt_i32_e32 vcc, v118, v119
	v_mov_b64_e32 v[170:171], s[24:25]
	v_mad_i64_i32 v[172:173], s[4:5], v181, s81, v[170:171]
	v_cndmask_b32_e32 v118, v210, v118, vcc
	v_lshlrev_b32_e32 v179, 2, v118
	global_load_dwordx4 v[120:123], v[116:117], off
	s_nop 0
	global_load_dwordx4 v[116:119], v[116:117], off offset:256
	v_add_u32_e32 v226, 0x80, v181
	v_mad_i64_i32 v[224:225], s[4:5], v226, s81, v[168:169]
	global_load_dwordx4 v[220:223], v[224:225], off
	s_nop 0
	global_load_dwordx4 v[224:227], v[224:225], off offset:256
	v_add_u32_e32 v234, 0x90, v181
	v_mad_i64_i32 v[232:233], s[4:5], v234, s81, v[168:169]
	global_load_dwordx4 v[228:231], v[232:233], off
	s_nop 0
	global_load_dwordx4 v[232:235], v[232:233], off offset:256
	v_add_u32_e32 v242, 0xa0, v181
	v_mad_i64_i32 v[240:241], s[4:5], v242, s81, v[168:169]
	global_load_dwordx4 v[236:239], v[240:241], off
	s_nop 0
	global_load_dwordx4 v[240:243], v[240:241], off offset:256
	v_add_u32_e32 v250, 0xb0, v181
	v_mad_i64_i32 v[248:249], s[4:5], v250, s81, v[168:169]
	global_load_dwordx4 v[244:247], v[248:249], off
	s_nop 0
	global_load_dwordx4 v[248:251], v[248:249], off offset:256
	v_lshl_add_u64 v[172:173], v[172:173], 0, v[166:167]
	v_cmp_lt_i32_e32 vcc, 0, v3
	s_waitcnt vmcnt(0)
	v_lshlrev_b32_e32 v186, 16, v182
	v_and_b32_e32 v187, 0xffff0000, v182
	v_lshlrev_b32_e32 v182, 16, v183
	v_and_b32_e32 v183, 0xffff0000, v183
	v_pk_fma_f32 v[142:143], v[142:143], 0.5, v[182:183] op_sel_hi:[1,0,1]
	v_lshlrev_b32_e32 v182, 16, v184
	v_and_b32_e32 v183, 0xffff0000, v184
	v_pk_fma_f32 v[182:183], v[136:137], 0.5, v[182:183] op_sel_hi:[1,0,1]
	v_lshlrev_b32_e32 v136, 16, v185
	v_and_b32_e32 v137, 0xffff0000, v185
	v_pk_fma_f32 v[140:141], v[140:141], 0.5, v[186:187] op_sel_hi:[1,0,1]
	v_pk_fma_f32 v[184:185], v[138:139], 0.5, v[136:137] op_sel_hi:[1,0,1]
	v_cvt_pk_bf16_f32 v136, v140, v141
	v_cvt_pk_bf16_f32 v137, v142, v143
	v_cvt_pk_bf16_f32 v138, v182, v183
	v_cvt_pk_bf16_f32 v139, v184, v185
	global_store_dwordx4 v[172:173], v[136:139], off
	v_pk_mul_f32 v[190:191], v[182:183], v[182:183]
	v_pk_mul_f32 v[192:193], v[184:185], v[184:185]
	v_lshlrev_b32_e32 v136, 16, v156
	v_and_b32_e32 v137, 0xffff0000, v156
	v_pk_fma_f32 v[128:129], v[128:129], 0.5, v[136:137] op_sel_hi:[1,0,1]
	v_lshlrev_b32_e32 v136, 16, v157
	v_and_b32_e32 v137, 0xffff0000, v157
	v_pk_fma_f32 v[130:131], v[130:131], 0.5, v[136:137] op_sel_hi:[1,0,1]
	v_lshlrev_b32_e32 v136, 16, v158
	v_and_b32_e32 v137, 0xffff0000, v158
	v_pk_fma_f32 v[136:137], v[124:125], 0.5, v[136:137] op_sel_hi:[1,0,1]
	v_lshlrev_b32_e32 v124, 16, v159
	v_and_b32_e32 v125, 0xffff0000, v159
	v_pk_fma_f32 v[138:139], v[126:127], 0.5, v[124:125] op_sel_hi:[1,0,1]
	v_pk_mul_f32 v[124:125], v[128:129], v[128:129]
	v_pk_mul_f32 v[126:127], v[130:131], v[130:131]
	v_add_f32_e32 v124, v124, v125
	v_add_f32_e32 v126, v126, v127
	v_pk_mul_f32 v[186:187], v[140:141], v[140:141]
	v_pk_mul_f32 v[188:189], v[142:143], v[142:143]
	v_pk_mul_f32 v[140:141], v[136:137], v[136:137]
	v_pk_mul_f32 v[142:143], v[138:139], v[138:139]
	v_add_f32_e32 v124, v124, v126
	v_add_f32_e32 v125, v192, v193
	v_add_f32_e32 v126, v190, v191
	v_add_f32_e32 v142, v142, v143
	v_add_f32_e32 v140, v140, v141
	v_add_f32_e32 v125, v126, v125
	v_add_f32_e32 v126, v188, v189
	v_add_f32_e32 v127, v186, v187
	v_add_f32_e32 v140, v140, v142
	v_add_f32_e32 v126, v127, v126
	v_add_f32_e32 v124, v124, v140
	v_add_f32_e32 v125, v126, v125
	v_add_f32_e32 v140, v125, v124
	v_cvt_pk_bf16_f32 v124, v128, v129
	v_lshlrev_b32_e32 v128, 16, v152
	v_and_b32_e32 v129, 0xffff0000, v152
	v_pk_fma_f32 v[112:113], v[112:113], 0.5, v[128:129] op_sel_hi:[1,0,1]
	v_lshlrev_b32_e32 v128, 16, v153
	v_and_b32_e32 v129, 0xffff0000, v153
	v_pk_fma_f32 v[114:115], v[114:115], 0.5, v[128:129] op_sel_hi:[1,0,1]
	v_lshlrev_b32_e32 v128, 16, v154
	v_and_b32_e32 v129, 0xffff0000, v154
	v_cvt_pk_bf16_f32 v125, v130, v131
	v_cvt_pk_bf16_f32 v126, v136, v137
	v_cvt_pk_bf16_f32 v127, v138, v139
	v_pk_fma_f32 v[128:129], v[108:109], 0.5, v[128:129] op_sel_hi:[1,0,1]
	v_lshlrev_b32_e32 v108, 16, v155
	v_and_b32_e32 v109, 0xffff0000, v155
	global_store_dwordx4 v[172:173], v[124:127], off offset:256
	v_pk_fma_f32 v[130:131], v[110:111], 0.5, v[108:109] op_sel_hi:[1,0,1]
	v_cvt_pk_bf16_f32 v108, v112, v113
	v_mad_i64_i32 v[126:127], s[4:5], v196, s81, v[170:171]
	v_lshl_add_u64 v[126:127], v[126:127], 0, v[166:167]
	v_cvt_pk_bf16_f32 v109, v114, v115
	v_cvt_pk_bf16_f32 v110, v128, v129
	v_cvt_pk_bf16_f32 v111, v130, v131
	ds_bpermute_b32 v124, v180, v140
	global_store_dwordx4 v[126:127], v[108:111], off
	v_pk_mul_f32 v[142:143], v[130:131], v[130:131]
	v_pk_mul_f32 v[136:137], v[112:113], v[112:113]
	v_lshlrev_b32_e32 v108, 16, v148
	v_and_b32_e32 v109, 0xffff0000, v148
	v_pk_fma_f32 v[104:105], v[104:105], 0.5, v[108:109] op_sel_hi:[1,0,1]
	v_lshlrev_b32_e32 v108, 16, v149
	v_and_b32_e32 v109, 0xffff0000, v149
	v_pk_fma_f32 v[106:107], v[106:107], 0.5, v[108:109] op_sel_hi:[1,0,1]
	v_lshlrev_b32_e32 v108, 16, v150
	v_and_b32_e32 v109, 0xffff0000, v150
	v_pk_fma_f32 v[108:109], v[100:101], 0.5, v[108:109] op_sel_hi:[1,0,1]
	v_lshlrev_b32_e32 v100, 16, v151
	v_and_b32_e32 v101, 0xffff0000, v151
	v_pk_fma_f32 v[110:111], v[102:103], 0.5, v[100:101] op_sel_hi:[1,0,1]
	v_pk_mul_f32 v[100:101], v[104:105], v[104:105]
	v_pk_mul_f32 v[102:103], v[106:107], v[106:107]
	s_waitcnt lgkmcnt(0)
; __device__ __forceinline__ unsigned cvt_pk_bf16(float lo, float hi) { f32x2_c v = {lo, hi}; bf16x2_c b = __builtin_convertvector(v, bf16x2_c); return __builtin_bit_cast(unsigned, b); }
; __device__ __forceinline__ float bf_lo(unsigned u) { return __uint_as_float(u << 16); }
; __device__ __forceinline__ float bf_hi(unsigned u) { return __uint_as_float(u & 0xffff0000u); }
;     __device__ __forceinline__ void operator()(const f32x4 (&acc)[2][2][4][2], const Unit& u, int wr, int wc, int fr, int fq) const {
;     ...
;             for (int m = 0; m < 4; ++m) { const int row = row0 + ai * HALF + m * 16; bf16_t* hp = Hx + (size_t)row * LDT + col0;
;                 float ss = 0.f;
; #pragma unroll
;                 for (int bj = 0; bj < 2; ++bj) { const u32x4 x = xv[m][bj]; const f32x4 a0 = acc[ai][bj][m][0], a1 = acc[ai][bj][m][1];
;                     const float y0 = bf_lo(x.x) + a0[0] * scale, y1 = bf_hi(x.x) + a0[1] * scale, y2 = bf_lo(x.y) + a0[2] * scale, y3 = bf_hi(x.y) + a0[3] * scale;
;                     const float y4 = bf_lo(x.z) + a1[0] * scale, y5 = bf_hi(x.z) + a1[1] * scale, y6 = bf_lo(x.w) + a1[2] * scale, y7 = bf_hi(x.w) + a1[3] * scale;
;                     ss += ((y0 * y0 + y1 * y1) + (y2 * y2 + y3 * y3)) + ((y4 * y4 + y5 * y5) + (y6 * y6 + y7 * y7));
;                     u32x4 w; w.x = cvt_pk_bf16(y0, y1); w.y = cvt_pk_bf16(y2, y3); w.z = cvt_pk_bf16(y4, y5); w.w = cvt_pk_bf16(y6, y7);
;                     *(u32x4*)(hp + bj * HALF) = w; }
;                 ss += __shfl_xor(ss, 16); ss += __shfl_xor(ss, 32); ssm[m] = ss; }
;             { const float sv = (fq == 0) ? ssm[0] : (fq == 1) ? ssm[1] : (fq == 2) ? ssm[2] : ssm[3];
	v_add_f32_e32 v124, v140, v124
	v_pk_mul_f32 v[140:141], v[128:129], v[128:129]
	v_add_f32_e32 v102, v102, v103
	v_add_f32_e32 v100, v100, v101
	v_pk_mul_f32 v[138:139], v[114:115], v[114:115]
	v_pk_mul_f32 v[112:113], v[108:109], v[108:109]
	v_pk_mul_f32 v[114:115], v[110:111], v[110:111]
	v_add_f32_e32 v100, v100, v102
	v_add_f32_e32 v101, v142, v143
	v_add_f32_e32 v102, v140, v141
	v_add_f32_e32 v114, v114, v115
	v_add_f32_e32 v112, v112, v113
	v_add_f32_e32 v101, v102, v101
	v_add_f32_e32 v102, v138, v139
	v_add_f32_e32 v103, v136, v137
	v_add_f32_e32 v112, v112, v114
	v_add_f32_e32 v102, v103, v102
	v_add_f32_e32 v100, v100, v112
	v_add_f32_e32 v101, v102, v101
	v_add_f32_e32 v112, v101, v100
	v_cvt_pk_bf16_f32 v100, v104, v105
	v_lshlrev_b32_e32 v104, 16, v144
	v_and_b32_e32 v105, 0xffff0000, v144
	v_pk_fma_f32 v[96:97], v[96:97], 0.5, v[104:105] op_sel_hi:[1,0,1]
	v_lshlrev_b32_e32 v104, 16, v145
	v_and_b32_e32 v105, 0xffff0000, v145
	v_pk_fma_f32 v[98:99], v[98:99], 0.5, v[104:105] op_sel_hi:[1,0,1]
	v_lshlrev_b32_e32 v104, 16, v146
	v_and_b32_e32 v105, 0xffff0000, v146
	v_cvt_pk_bf16_f32 v101, v106, v107
	v_cvt_pk_bf16_f32 v102, v108, v109
	v_cvt_pk_bf16_f32 v103, v110, v111
	v_pk_fma_f32 v[104:105], v[92:93], 0.5, v[104:105] op_sel_hi:[1,0,1]
	v_lshlrev_b32_e32 v92, 16, v147
	v_and_b32_e32 v93, 0xffff0000, v147
	global_store_dwordx4 v[126:127], v[100:103], off offset:256
	v_pk_fma_f32 v[106:107], v[94:95], 0.5, v[92:93] op_sel_hi:[1,0,1]
	v_cvt_pk_bf16_f32 v92, v96, v97
	v_mad_i64_i32 v[102:103], s[4:5], v195, s81, v[170:171]
	v_lshl_add_u64 v[102:103], v[102:103], 0, v[166:167]
	v_cvt_pk_bf16_f32 v93, v98, v99
	v_cvt_pk_bf16_f32 v94, v104, v105
	v_cvt_pk_bf16_f32 v95, v106, v107
	ds_bpermute_b32 v100, v180, v112
	global_store_dwordx4 v[102:103], v[92:95], off
	v_pk_mul_f32 v[114:115], v[106:107], v[106:107]
	v_pk_mul_f32 v[108:109], v[96:97], v[96:97]
	v_lshlrev_b32_e32 v92, 16, v132
	v_and_b32_e32 v93, 0xffff0000, v132
	v_pk_fma_f32 v[88:89], v[88:89], 0.5, v[92:93] op_sel_hi:[1,0,1]
	v_lshlrev_b32_e32 v92, 16, v133
	v_and_b32_e32 v93, 0xffff0000, v133
	v_pk_fma_f32 v[90:91], v[90:91], 0.5, v[92:93] op_sel_hi:[1,0,1]
	v_lshlrev_b32_e32 v92, 16, v134
	v_and_b32_e32 v93, 0xffff0000, v134
	v_pk_fma_f32 v[92:93], v[84:85], 0.5, v[92:93] op_sel_hi:[1,0,1]
	v_lshlrev_b32_e32 v84, 16, v135
	v_and_b32_e32 v85, 0xffff0000, v135
	v_pk_fma_f32 v[94:95], v[86:87], 0.5, v[84:85] op_sel_hi:[1,0,1]
	v_pk_mul_f32 v[84:85], v[88:89], v[88:89]
	v_pk_mul_f32 v[86:87], v[90:91], v[90:91]
	s_waitcnt lgkmcnt(0)
	v_add_f32_e32 v100, v112, v100
	v_pk_mul_f32 v[112:113], v[104:105], v[104:105]
	v_add_f32_e32 v86, v86, v87
	v_add_f32_e32 v84, v84, v85
	v_pk_mul_f32 v[110:111], v[98:99], v[98:99]
	v_pk_mul_f32 v[96:97], v[92:93], v[92:93]
	v_pk_mul_f32 v[98:99], v[94:95], v[94:95]
	v_add_f32_e32 v84, v84, v86
	v_add_f32_e32 v85, v114, v115
	v_add_f32_e32 v86, v112, v113
	v_add_f32_e32 v98, v98, v99
	v_add_f32_e32 v96, v96, v97
	v_add_f32_e32 v85, v86, v85
	v_add_f32_e32 v86, v110, v111
	v_add_f32_e32 v87, v108, v109
	v_add_f32_e32 v96, v96, v98
	v_add_f32_e32 v86, v87, v86
	v_add_f32_e32 v84, v84, v96
	v_add_f32_e32 v85, v86, v85
	v_add_f32_e32 v96, v85, v84
	v_cvt_pk_bf16_f32 v84, v88, v89
	v_lshlrev_b32_e32 v88, 16, v120
	v_and_b32_e32 v89, 0xffff0000, v120
	v_pk_fma_f32 v[80:81], v[80:81], 0.5, v[88:89] op_sel_hi:[1,0,1]
	v_lshlrev_b32_e32 v88, 16, v121
	v_and_b32_e32 v89, 0xffff0000, v121
	v_pk_fma_f32 v[82:83], v[82:83], 0.5, v[88:89] op_sel_hi:[1,0,1]
	v_lshlrev_b32_e32 v88, 16, v122
	v_and_b32_e32 v89, 0xffff0000, v122
	v_cvt_pk_bf16_f32 v85, v90, v91
	v_cvt_pk_bf16_f32 v86, v92, v93
	v_cvt_pk_bf16_f32 v87, v94, v95
	v_pk_fma_f32 v[88:89], v[76:77], 0.5, v[88:89] op_sel_hi:[1,0,1]
	v_lshlrev_b32_e32 v76, 16, v123
	v_and_b32_e32 v77, 0xffff0000, v123
	global_store_dwordx4 v[102:103], v[84:87], off offset:256
	v_pk_fma_f32 v[90:91], v[78:79], 0.5, v[76:77] op_sel_hi:[1,0,1]
	v_cvt_pk_bf16_f32 v76, v80, v81
	v_mad_i64_i32 v[86:87], s[4:5], v194, s81, v[170:171]
	v_lshl_add_u64 v[86:87], v[86:87], 0, v[166:167]
	v_cvt_pk_bf16_f32 v77, v82, v83
	v_cvt_pk_bf16_f32 v78, v88, v89
	v_cvt_pk_bf16_f32 v79, v90, v91
	ds_bpermute_b32 v84, v180, v96
	global_store_dwordx4 v[86:87], v[76:79], off
	v_pk_mul_f32 v[98:99], v[90:91], v[90:91]
	v_pk_mul_f32 v[92:93], v[80:81], v[80:81]
	v_lshlrev_b32_e32 v76, 16, v116
	v_and_b32_e32 v77, 0xffff0000, v116
	v_pk_fma_f32 v[72:73], v[72:73], 0.5, v[76:77] op_sel_hi:[1,0,1]
	v_lshlrev_b32_e32 v76, 16, v117
	v_and_b32_e32 v77, 0xffff0000, v117
	v_pk_fma_f32 v[74:75], v[74:75], 0.5, v[76:77] op_sel_hi:[1,0,1]
	v_lshlrev_b32_e32 v76, 16, v118
	v_and_b32_e32 v77, 0xffff0000, v118
	v_pk_fma_f32 v[76:77], v[68:69], 0.5, v[76:77] op_sel_hi:[1,0,1]
	v_lshlrev_b32_e32 v68, 16, v119
	v_and_b32_e32 v69, 0xffff0000, v119
	v_pk_fma_f32 v[78:79], v[70:71], 0.5, v[68:69] op_sel_hi:[1,0,1]
	v_pk_mul_f32 v[68:69], v[72:73], v[72:73]
	v_pk_mul_f32 v[70:71], v[74:75], v[74:75]
	s_waitcnt lgkmcnt(0)
	v_add_f32_e32 v84, v96, v84
	v_pk_mul_f32 v[96:97], v[88:89], v[88:89]
	v_add_f32_e32 v70, v70, v71
	v_add_f32_e32 v68, v68, v69
	v_pk_mul_f32 v[94:95], v[82:83], v[82:83]
	v_pk_mul_f32 v[80:81], v[76:77], v[76:77]
	v_pk_mul_f32 v[82:83], v[78:79], v[78:79]
	v_add_f32_e32 v68, v68, v70
	v_add_f32_e32 v69, v98, v99
	v_add_f32_e32 v70, v96, v97
	v_add_f32_e32 v82, v82, v83
	v_add_f32_e32 v80, v80, v81
	v_add_f32_e32 v69, v70, v69
	v_add_f32_e32 v70, v94, v95
	v_add_f32_e32 v71, v92, v93
	v_add_f32_e32 v80, v80, v82
	v_add_f32_e32 v70, v71, v70
	v_add_f32_e32 v68, v68, v80
	v_add_f32_e32 v69, v70, v69
	v_add_f32_e32 v80, v69, v68
	v_cvt_pk_bf16_f32 v68, v72, v73
	v_cvt_pk_bf16_f32 v69, v74, v75
	v_cvt_pk_bf16_f32 v70, v76, v77
	v_cvt_pk_bf16_f32 v71, v78, v79
	global_store_dwordx4 v[86:87], v[68:71], off offset:256
	ds_bpermute_b32 v68, v180, v80
	ds_bpermute_b32 v125, v179, v124
	ds_bpermute_b32 v101, v179, v100
	ds_bpermute_b32 v85, v179, v84
	s_waitcnt lgkmcnt(3)
	v_add_f32_e32 v69, v80, v68
	ds_bpermute_b32 v70, v179, v69
	s_and_saveexec_b64 s[4:5], vcc
	s_xor_b64 s[4:5], exec, s[4:5]
	s_cbranch_execz .LBB0_242
	v_cmp_ne_u32_e32 vcc, 1, v3
	s_and_saveexec_b64 s[24:25], vcc
	s_xor_b64 s[24:25], exec, s[24:25]
	s_cbranch_execz .LBB0_239
	s_waitcnt lgkmcnt(0)
	v_add_f32_e32 v68, v69, v70
	v_add_f32_e32 v69, v84, v85
	v_cndmask_b32_e64 v68, v68, v69, s[6:7]

; __device__ __forceinline__ unsigned cvt_pk_bf16(float lo, float hi) { f32x2_c v = {lo, hi}; bf16x2_c b = __builtin_convertvector(v, bf16x2_c); return __builtin_bit_cast(unsigned, b); }
; __device__ __forceinline__ float bf_lo(unsigned u) { return __uint_as_float(u << 16); }
; __device__ __forceinline__ float bf_hi(unsigned u) { return __uint_as_float(u & 0xffff0000u); }
;     __device__ __forceinline__ void operator()(const f32x4 (&acc)[2][2][4][2], const Unit& u, int wr, int wc, int fr, int fq) const {
;     ...
;                 for (int bj = 0; bj < 2; ++bj) xv[m][bj] = *(const u32x4*)(Hx + (size_t)(row0 + ai * HALF + m * 16) * LDT + col0 + bj * HALF);
;             float ssm[4];
; #pragma unroll
;             for (int m = 0; m < 4; ++m) { const int row = row0 + ai * HALF + m * 16; bf16_t* hp = Hx + (size_t)row * LDT + col0;
;                 float ss = 0.f;
; #pragma unroll
;                 for (int bj = 0; bj < 2; ++bj) { const u32x4 x = xv[m][bj]; const f32x4 a0 = acc[ai][bj][m][0], a1 = acc[ai][bj][m][1];
;                     const float y0 = bf_lo(x.x) + a0[0] * scale, y1 = bf_hi(x.x) + a0[1] * scale, y2 = bf_lo(x.y) + a0[2] * scale, y3 = bf_hi(x.y) + a0[3] * scale;
;                     const float y4 = bf_lo(x.z) + a1[0] * scale, y5 = bf_hi(x.z) + a1[1] * scale, y6 = bf_lo(x.w) + a1[2] * scale, y7 = bf_hi(x.w) + a1[3] * scale;
;                     ss += ((y0 * y0 + y1 * y1) + (y2 * y2 + y3 * y3)) + ((y4 * y4 + y5 * y5) + (y6 * y6 + y7 * y7));
;                     u32x4 w; w.x = cvt_pk_bf16(y0, y1); w.y = cvt_pk_bf16(y2, y3); w.z = cvt_pk_bf16(y4, y5); w.w = cvt_pk_bf16(y6, y7);
;                     *(u32x4*)(hp + bj * HALF) = w; }
;                 ss += __shfl_xor(ss, 16); ss += __shfl_xor(ss, 32); ssm[m] = ss; }
;             { const float sv = (fq == 0) ? ssm[0] : (fq == 1) ? ssm[1] : (fq == 2) ? ssm[2] : ssm[3];
;               ssq[(size_t)(row0 + ai * HALF + fq * 16) * 32 + u.pn * 4 + wc] = sv; }
.LBB0_244:
	s_or_b64 exec, exec, s[4:5]
	v_or_b32_e32 v92, v181, v175
	v_ashrrev_i32_e32 v93, 31, v92
	s_lshl_b32 s24, s2, 2
	s_waitcnt lgkmcnt(0)
	v_lshlrev_b64 v[70:71], 7, v[92:93]
	s_ashr_i32 s25, s24, 31
	v_lshl_add_u64 v[70:71], s[16:17], 0, v[70:71]
	v_lshl_add_u64 v[70:71], s[24:25], 2, v[70:71]
	s_lshl_b32 s0, s15, 2
	v_lshl_add_u64 v[70:71], v[70:71], 0, s[0:1]
	global_store_dword v[70:71], v68, off
	v_add_u32_e32 v97, 0x80, v181
	v_mad_i64_i32 v[68:69], s[2:3], v97, s81, v[168:169]
	v_add_u32_e32 v116, 0x90, v181
	v_mad_i64_i32 v[68:69], s[2:3], v116, s81, v[168:169]
	v_add_u32_e32 v96, 0xa0, v181
	v_mad_i64_i32 v[68:69], s[2:3], v96, s81, v[168:169]
	v_add_u32_e32 v93, 0xb0, v181
	v_mad_i64_i32 v[68:69], s[2:3], v93, s81, v[168:169]
	s_nop 0
	v_readlane_b32 s2, v254, 23
	v_readlane_b32 s3, v254, 24
	v_cmp_lt_i32_e32 vcc, 0, v3
	v_lshlrev_b32_e32 v108, 16, v220
	v_and_b32_e32 v109, 0xffff0000, v220
	v_lshlrev_b32_e32 v98, 16, v221
	v_and_b32_e32 v99, 0xffff0000, v221
	v_pk_fma_f32 v[58:59], v[58:59], 0.5, v[98:99] op_sel_hi:[1,0,1]
	v_lshlrev_b32_e32 v98, 16, v222
	v_and_b32_e32 v99, 0xffff0000, v222
	v_mov_b64_e32 v[94:95], s[2:3]
	v_pk_fma_f32 v[98:99], v[52:53], 0.5, v[98:99] op_sel_hi:[1,0,1]
	v_lshlrev_b32_e32 v52, 16, v223
	v_and_b32_e32 v53, 0xffff0000, v223
	v_mad_i64_i32 v[106:107], s[2:3], v97, s81, v[94:95]
	v_pk_fma_f32 v[56:57], v[56:57], 0.5, v[108:109] op_sel_hi:[1,0,1]
	v_pk_fma_f32 v[100:101], v[54:55], 0.5, v[52:53] op_sel_hi:[1,0,1]
	v_lshl_add_u64 v[106:107], v[106:107], 0, v[166:167]
	v_cvt_pk_bf16_f32 v52, v56, v57
	v_cvt_pk_bf16_f32 v53, v58, v59
	v_cvt_pk_bf16_f32 v54, v98, v99
	v_cvt_pk_bf16_f32 v55, v100, v101
	global_store_dwordx4 v[106:107], v[52:55], off
	v_pk_mul_f32 v[108:109], v[56:57], v[56:57]
	v_pk_mul_f32 v[110:111], v[58:59], v[58:59]
	v_lshlrev_b32_e32 v52, 16, v224
	v_and_b32_e32 v53, 0xffff0000, v224
	v_lshlrev_b32_e32 v54, 16, v225
	v_and_b32_e32 v55, 0xffff0000, v225
	v_pk_fma_f32 v[52:53], v[64:65], 0.5, v[52:53] op_sel_hi:[1,0,1]
	v_pk_fma_f32 v[54:55], v[66:67], 0.5, v[54:55] op_sel_hi:[1,0,1]
	v_lshlrev_b32_e32 v56, 16, v226
	v_and_b32_e32 v57, 0xffff0000, v226
	v_lshlrev_b32_e32 v58, 16, v227
	v_and_b32_e32 v59, 0xffff0000, v227
	v_pk_fma_f32 v[56:57], v[60:61], 0.5, v[56:57] op_sel_hi:[1,0,1]
	v_pk_fma_f32 v[58:59], v[62:63], 0.5, v[58:59] op_sel_hi:[1,0,1]
	v_pk_mul_f32 v[60:61], v[52:53], v[52:53]
	v_pk_mul_f32 v[62:63], v[54:55], v[54:55]
	v_pk_mul_f32 v[112:113], v[98:99], v[98:99]
	v_pk_mul_f32 v[114:115], v[100:101], v[100:101]
	v_add_f32_e32 v62, v62, v63
	v_add_f32_e32 v60, v60, v61
	v_pk_mul_f32 v[64:65], v[56:57], v[56:57]
	v_pk_mul_f32 v[66:67], v[58:59], v[58:59]
	v_add_f32_e32 v60, v60, v62
	v_add_f32_e32 v61, v114, v115
	v_add_f32_e32 v62, v112, v113
	v_add_f32_e32 v66, v66, v67
	v_add_f32_e32 v64, v64, v65
	v_add_f32_e32 v61, v62, v61
	v_add_f32_e32 v62, v110, v111
	v_add_f32_e32 v63, v108, v109
	v_add_f32_e32 v64, v64, v66
	v_add_f32_e32 v62, v63, v62
	v_add_f32_e32 v60, v60, v64
	v_add_f32_e32 v61, v62, v61
	v_add_f32_e32 v60, v61, v60
	v_cvt_pk_bf16_f32 v52, v52, v53
	v_cvt_pk_bf16_f32 v53, v54, v55
	v_cvt_pk_bf16_f32 v54, v56, v57
	v_cvt_pk_bf16_f32 v55, v58, v59
	global_store_dwordx4 v[106:107], v[52:55], off offset:256
	ds_bpermute_b32 v52, v180, v60
	v_lshlrev_b32_e32 v56, 16, v228
	v_and_b32_e32 v57, 0xffff0000, v228
	v_pk_fma_f32 v[48:49], v[48:49], 0.5, v[56:57] op_sel_hi:[1,0,1]
	v_lshlrev_b32_e32 v56, 16, v229
	v_and_b32_e32 v57, 0xffff0000, v229
	v_pk_fma_f32 v[50:51], v[50:51], 0.5, v[56:57] op_sel_hi:[1,0,1]
	v_lshlrev_b32_e32 v56, 16, v230
	v_and_b32_e32 v57, 0xffff0000, v230
	v_pk_fma_f32 v[56:57], v[44:45], 0.5, v[56:57] op_sel_hi:[1,0,1]
	v_lshlrev_b32_e32 v44, 16, v231
	v_and_b32_e32 v45, 0xffff0000, v231
	s_waitcnt lgkmcnt(0)
	v_add_f32_e32 v54, v60, v52
	v_mad_i64_i32 v[52:53], s[2:3], v116, s81, v[94:95]
	v_pk_fma_f32 v[58:59], v[46:47], 0.5, v[44:45] op_sel_hi:[1,0,1]
	v_lshl_add_u64 v[52:53], v[52:53], 0, v[166:167]
	v_cvt_pk_bf16_f32 v44, v48, v49
	v_cvt_pk_bf16_f32 v45, v50, v51
	v_cvt_pk_bf16_f32 v46, v56, v57
	v_cvt_pk_bf16_f32 v47, v58, v59
	global_store_dwordx4 v[52:53], v[44:47], off
	v_pk_mul_f32 v[64:65], v[56:57], v[56:57]
	v_pk_mul_f32 v[66:67], v[58:59], v[58:59]
	v_lshlrev_b32_e32 v44, 16, v232
	v_and_b32_e32 v45, 0xffff0000, v232
	v_pk_fma_f32 v[40:41], v[40:41], 0.5, v[44:45] op_sel_hi:[1,0,1]
	v_lshlrev_b32_e32 v44, 16, v233
	v_and_b32_e32 v45, 0xffff0000, v233
	v_pk_fma_f32 v[42:43], v[42:43], 0.5, v[44:45] op_sel_hi:[1,0,1]
	v_lshlrev_b32_e32 v44, 16, v234
	v_and_b32_e32 v45, 0xffff0000, v234
	v_pk_fma_f32 v[44:45], v[36:37], 0.5, v[44:45] op_sel_hi:[1,0,1]
	v_lshlrev_b32_e32 v36, 16, v235
	v_and_b32_e32 v37, 0xffff0000, v235
	v_pk_fma_f32 v[46:47], v[38:39], 0.5, v[36:37] op_sel_hi:[1,0,1]
	v_pk_mul_f32 v[36:37], v[40:41], v[40:41]
	v_pk_mul_f32 v[38:39], v[42:43], v[42:43]
	v_add_f32_e32 v36, v36, v37
	v_add_f32_e32 v38, v38, v39
	v_pk_mul_f32 v[60:61], v[48:49], v[48:49]
	v_pk_mul_f32 v[62:63], v[50:51], v[50:51]
	v_pk_mul_f32 v[48:49], v[44:45], v[44:45]
	v_pk_mul_f32 v[50:51], v[46:47], v[46:47]
	v_add_f32_e32 v36, v36, v38
	v_add_f32_e32 v37, v66, v67
	v_add_f32_e32 v38, v64, v65
	v_add_f32_e32 v50, v50, v51
	v_add_f32_e32 v48, v48, v49
	v_add_f32_e32 v37, v38, v37
	v_add_f32_e32 v38, v62, v63
	v_add_f32_e32 v39, v60, v61
	v_add_f32_e32 v48, v48, v50
	v_add_f32_e32 v38, v39, v38
	v_add_f32_e32 v36, v36, v48
	v_add_f32_e32 v37, v38, v37
	v_add_f32_e32 v48, v37, v36
; __device__ __forceinline__ unsigned cvt_pk_bf16(float lo, float hi) { f32x2_c v = {lo, hi}; bf16x2_c b = __builtin_convertvector(v, bf16x2_c); return __builtin_bit_cast(unsigned, b); }
; __device__ __forceinline__ float bf_lo(unsigned u) { return __uint_as_float(u << 16); }
; __device__ __forceinline__ float bf_hi(unsigned u) { return __uint_as_float(u & 0xffff0000u); }
;     __device__ __forceinline__ void operator()(const f32x4 (&acc)[2][2][4][2], const Unit& u, int wr, int wc, int fr, int fq) const {
;     ...
;             for (int m = 0; m < 4; ++m) { const int row = row0 + ai * HALF + m * 16; bf16_t* hp = Hx + (size_t)row * LDT + col0;
;                 float ss = 0.f;
; #pragma unroll
;                 for (int bj = 0; bj < 2; ++bj) { const u32x4 x = xv[m][bj]; const f32x4 a0 = acc[ai][bj][m][0], a1 = acc[ai][bj][m][1];
;                     const float y0 = bf_lo(x.x) + a0[0] * scale, y1 = bf_hi(x.x) + a0[1] * scale, y2 = bf_lo(x.y) + a0[2] * scale, y3 = bf_hi(x.y) + a0[3] * scale;
;                     const float y4 = bf_lo(x.z) + a1[0] * scale, y5 = bf_hi(x.z) + a1[1] * scale, y6 = bf_lo(x.w) + a1[2] * scale, y7 = bf_hi(x.w) + a1[3] * scale;
;                     ss += ((y0 * y0 + y1 * y1) + (y2 * y2 + y3 * y3)) + ((y4 * y4 + y5 * y5) + (y6 * y6 + y7 * y7));
;                     u32x4 w; w.x = cvt_pk_bf16(y0, y1); w.y = cvt_pk_bf16(y2, y3); w.z = cvt_pk_bf16(y4, y5); w.w = cvt_pk_bf16(y6, y7);
;                     *(u32x4*)(hp + bj * HALF) = w; }
;                 ss += __shfl_xor(ss, 16); ss += __shfl_xor(ss, 32); ssm[m] = ss; }
;             { const float sv = (fq == 0) ? ssm[0] : (fq == 1) ? ssm[1] : (fq == 2) ? ssm[2] : ssm[3];
	v_cvt_pk_bf16_f32 v36, v40, v41
	v_lshlrev_b32_e32 v40, 16, v236
	v_and_b32_e32 v41, 0xffff0000, v236
	v_pk_fma_f32 v[32:33], v[32:33], 0.5, v[40:41] op_sel_hi:[1,0,1]
	v_lshlrev_b32_e32 v40, 16, v237
	v_and_b32_e32 v41, 0xffff0000, v237
	v_pk_fma_f32 v[34:35], v[34:35], 0.5, v[40:41] op_sel_hi:[1,0,1]
	v_lshlrev_b32_e32 v40, 16, v238
	v_and_b32_e32 v41, 0xffff0000, v238
	v_cvt_pk_bf16_f32 v37, v42, v43
	v_cvt_pk_bf16_f32 v38, v44, v45
	v_cvt_pk_bf16_f32 v39, v46, v47
	v_pk_fma_f32 v[40:41], v[28:29], 0.5, v[40:41] op_sel_hi:[1,0,1]
	v_lshlrev_b32_e32 v28, 16, v239
	v_and_b32_e32 v29, 0xffff0000, v239
	global_store_dwordx4 v[52:53], v[36:39], off offset:256
	v_pk_fma_f32 v[42:43], v[30:31], 0.5, v[28:29] op_sel_hi:[1,0,1]
	v_cvt_pk_bf16_f32 v28, v32, v33
	v_mad_i64_i32 v[38:39], s[2:3], v96, s81, v[94:95]
	v_lshl_add_u64 v[38:39], v[38:39], 0, v[166:167]
	v_cvt_pk_bf16_f32 v29, v34, v35
	v_cvt_pk_bf16_f32 v30, v40, v41
	v_cvt_pk_bf16_f32 v31, v42, v43
	ds_bpermute_b32 v36, v180, v48
	global_store_dwordx4 v[38:39], v[28:31], off
	v_pk_mul_f32 v[50:51], v[42:43], v[42:43]
	v_pk_mul_f32 v[44:45], v[32:33], v[32:33]
	v_lshlrev_b32_e32 v28, 16, v240
	v_and_b32_e32 v29, 0xffff0000, v240
	v_pk_fma_f32 v[24:25], v[24:25], 0.5, v[28:29] op_sel_hi:[1,0,1]
	v_lshlrev_b32_e32 v28, 16, v241
	v_and_b32_e32 v29, 0xffff0000, v241
	v_pk_fma_f32 v[26:27], v[26:27], 0.5, v[28:29] op_sel_hi:[1,0,1]
	v_lshlrev_b32_e32 v28, 16, v242
	v_and_b32_e32 v29, 0xffff0000, v242
	v_pk_fma_f32 v[28:29], v[20:21], 0.5, v[28:29] op_sel_hi:[1,0,1]
	v_lshlrev_b32_e32 v20, 16, v243
	v_and_b32_e32 v21, 0xffff0000, v243
	v_pk_fma_f32 v[30:31], v[22:23], 0.5, v[20:21] op_sel_hi:[1,0,1]
	v_pk_mul_f32 v[20:21], v[24:25], v[24:25]
	v_pk_mul_f32 v[22:23], v[26:27], v[26:27]
	s_waitcnt lgkmcnt(0)
	v_add_f32_e32 v36, v48, v36
	v_pk_mul_f32 v[48:49], v[40:41], v[40:41]
	v_add_f32_e32 v22, v22, v23
	v_add_f32_e32 v20, v20, v21
	v_pk_mul_f32 v[46:47], v[34:35], v[34:35]
	v_pk_mul_f32 v[32:33], v[28:29], v[28:29]
	v_pk_mul_f32 v[34:35], v[30:31], v[30:31]
	v_add_f32_e32 v20, v20, v22
	v_add_f32_e32 v21, v50, v51
	v_add_f32_e32 v22, v48, v49
	v_add_f32_e32 v34, v34, v35
	v_add_f32_e32 v32, v32, v33
	v_add_f32_e32 v21, v22, v21
	v_add_f32_e32 v22, v46, v47
	v_add_f32_e32 v23, v44, v45
	v_add_f32_e32 v32, v32, v34
	v_add_f32_e32 v22, v23, v22
	v_add_f32_e32 v20, v20, v32
	v_add_f32_e32 v21, v22, v21
	v_add_f32_e32 v32, v21, v20
	v_cvt_pk_bf16_f32 v20, v24, v25
	v_lshlrev_b32_e32 v24, 16, v244
	v_and_b32_e32 v25, 0xffff0000, v244
	v_pk_fma_f32 v[16:17], v[16:17], 0.5, v[24:25] op_sel_hi:[1,0,1]
	v_lshlrev_b32_e32 v24, 16, v245
	v_and_b32_e32 v25, 0xffff0000, v245
	v_pk_fma_f32 v[18:19], v[18:19], 0.5, v[24:25] op_sel_hi:[1,0,1]
	v_lshlrev_b32_e32 v24, 16, v246
	v_and_b32_e32 v25, 0xffff0000, v246
	v_cvt_pk_bf16_f32 v21, v26, v27
	v_cvt_pk_bf16_f32 v22, v28, v29
	v_cvt_pk_bf16_f32 v23, v30, v31
	v_pk_fma_f32 v[24:25], v[12:13], 0.5, v[24:25] op_sel_hi:[1,0,1]
	v_lshlrev_b32_e32 v12, 16, v247
	v_and_b32_e32 v13, 0xffff0000, v247
	global_store_dwordx4 v[38:39], v[20:23], off offset:256
	v_pk_fma_f32 v[26:27], v[14:15], 0.5, v[12:13] op_sel_hi:[1,0,1]
	v_cvt_pk_bf16_f32 v12, v16, v17
	v_mad_i64_i32 v[22:23], s[2:3], v93, s81, v[94:95]
	v_lshl_add_u64 v[22:23], v[22:23], 0, v[166:167]
	v_cvt_pk_bf16_f32 v13, v18, v19
	v_cvt_pk_bf16_f32 v14, v24, v25
	v_cvt_pk_bf16_f32 v15, v26, v27
	ds_bpermute_b32 v20, v180, v32
	global_store_dwordx4 v[22:23], v[12:15], off
	v_pk_mul_f32 v[34:35], v[26:27], v[26:27]
	v_pk_mul_f32 v[28:29], v[16:17], v[16:17]
	v_lshlrev_b32_e32 v12, 16, v248
	v_and_b32_e32 v13, 0xffff0000, v248
	v_pk_fma_f32 v[8:9], v[8:9], 0.5, v[12:13] op_sel_hi:[1,0,1]
	v_lshlrev_b32_e32 v12, 16, v249
	v_and_b32_e32 v13, 0xffff0000, v249
	v_pk_fma_f32 v[10:11], v[10:11], 0.5, v[12:13] op_sel_hi:[1,0,1]
	v_lshlrev_b32_e32 v12, 16, v250
	v_and_b32_e32 v13, 0xffff0000, v250
	v_pk_fma_f32 v[12:13], v[4:5], 0.5, v[12:13] op_sel_hi:[1,0,1]
	v_lshlrev_b32_e32 v4, 16, v251
	v_and_b32_e32 v5, 0xffff0000, v251
	v_pk_fma_f32 v[14:15], v[6:7], 0.5, v[4:5] op_sel_hi:[1,0,1]
	v_pk_mul_f32 v[4:5], v[8:9], v[8:9]
	v_pk_mul_f32 v[6:7], v[10:11], v[10:11]
	s_waitcnt lgkmcnt(0)
	v_add_f32_e32 v20, v32, v20
	v_pk_mul_f32 v[32:33], v[24:25], v[24:25]
	v_add_f32_e32 v6, v6, v7
	v_add_f32_e32 v4, v4, v5
	v_pk_mul_f32 v[30:31], v[18:19], v[18:19]
	v_pk_mul_f32 v[16:17], v[12:13], v[12:13]
	v_pk_mul_f32 v[18:19], v[14:15], v[14:15]
	v_add_f32_e32 v4, v4, v6
	v_add_f32_e32 v5, v34, v35
	v_add_f32_e32 v6, v32, v33
	v_add_f32_e32 v18, v18, v19
	v_add_f32_e32 v16, v16, v17
	v_add_f32_e32 v5, v6, v5
	v_add_f32_e32 v6, v30, v31
	v_add_f32_e32 v7, v28, v29
	v_add_f32_e32 v16, v16, v18
	v_add_f32_e32 v6, v7, v6
	v_add_f32_e32 v4, v4, v16
	v_add_f32_e32 v5, v6, v5
	v_add_f32_e32 v16, v5, v4
	v_cvt_pk_bf16_f32 v4, v8, v9
	v_cvt_pk_bf16_f32 v5, v10, v11
	v_cvt_pk_bf16_f32 v6, v12, v13
	v_cvt_pk_bf16_f32 v7, v14, v15
	global_store_dwordx4 v[22:23], v[4:7], off offset:256
	ds_bpermute_b32 v4, v180, v16
	ds_bpermute_b32 v55, v179, v54
	ds_bpermute_b32 v37, v179, v36
	ds_bpermute_b32 v21, v179, v20
	s_waitcnt lgkmcnt(3)
	v_add_f32_e32 v5, v16, v4
	ds_bpermute_b32 v6, v179, v5
	s_and_saveexec_b64 s[2:3], vcc
	s_xor_b64 s[4:5], exec, s[2:3]
	s_cbranch_execz .LBB0_250
	v_cmp_ne_u32_e32 vcc, 1, v3
	s_and_saveexec_b64 s[2:3], vcc
	s_xor_b64 s[26:27], exec, s[2:3]
	s_cbranch_execz .LBB0_247
	s_waitcnt lgkmcnt(0)
	v_add_f32_e32 v4, v5, v6
	v_add_f32_e32 v5, v20, v21
	v_cndmask_b32_e64 v4, v4, v5, s[6:7]

; __device__ __forceinline__ unsigned cvt_pk_bf16(float lo, float hi) { f32x2_c v = {lo, hi}; bf16x2_c b = __builtin_convertvector(v, bf16x2_c); return __builtin_bit_cast(unsigned, b); }
; __device__ __forceinline__ float bf_lo(unsigned u) { return __uint_as_float(u << 16); }
; __device__ __forceinline__ float bf_hi(unsigned u) { return __uint_as_float(u & 0xffff0000u); }
;     __device__ __forceinline__ void operator()(const f32x4 (&acc)[2][2][4][2], const Unit& u, int wr, int wc, int fr, int fq) const {
;     ...
;         for (int ai = 0; ai < 2; ++ai) {
;             u32x4 xv[4][2];
; #pragma unroll
;             for (int m = 0; m < 4; ++m)
; #pragma unroll
;                 for (int bj = 0; bj < 2; ++bj) xv[m][bj] = *(const u32x4*)(Hx + (size_t)(row0 + ai * HALF + m * 16) * LDT + col0 + bj * HALF);
;             float ssm[4];
; #pragma unroll
;             for (int m = 0; m < 4; ++m) { const int row = row0 + ai * HALF + m * 16; bf16_t* hp = Hx + (size_t)row * LDT + col0;
;                 float ss = 0.f;
; #pragma unroll
;                 for (int bj = 0; bj < 2; ++bj) { const u32x4 x = xv[m][bj]; const f32x4 a0 = acc[ai][bj][m][0], a1 = acc[ai][bj][m][1];
;                     const float y0 = bf_lo(x.x) + a0[0] * scale, y1 = bf_hi(x.x) + a0[1] * scale, y2 = bf_lo(x.y) + a0[2] * scale, y3 = bf_hi(x.y) + a0[3] * scale;
;                     const float y4 = bf_lo(x.z) + a1[0] * scale, y5 = bf_hi(x.z) + a1[1] * scale, y6 = bf_lo(x.w) + a1[2] * scale, y7 = bf_hi(x.w) + a1[3] * scale;
;                     ss += ((y0 * y0 + y1 * y1) + (y2 * y2 + y3 * y3)) + ((y4 * y4 + y5 * y5) + (y6 * y6 + y7 * y7));
;                     u32x4 w; w.x = cvt_pk_bf16(y0, y1); w.y = cvt_pk_bf16(y2, y3); w.z = cvt_pk_bf16(y4, y5); w.w = cvt_pk_bf16(y6, y7);
;                     *(u32x4*)(hp + bj * HALF) = w; }
.LBB0_703:
	v_lshl_or_b32 v116, s0, 8, v177
	v_ashrrev_i32_e32 v117, 31, v116
	v_readlane_b32 s4, v254, 23
	v_lshlrev_b64 v[166:167], 1, v[116:117]
	v_readlane_b32 s5, v254, 24
	v_lshl_add_u32 v181, s2, 8, v174
	v_or_b32_e32 v196, 16, v181
	v_lshl_add_u64 v[168:169], s[4:5], 0, v[166:167]
	v_mad_i64_i32 v[116:117], s[2:3], v181, s81, v[168:169]
	global_load_dwordx4 v[182:185], v[116:117], off
	global_load_dwordx4 v[156:159], v[116:117], off offset:256
	v_mad_i64_i32 v[116:117], s[2:3], v196, s81, v[168:169]
	global_load_dwordx4 v[152:155], v[116:117], off
	global_load_dwordx4 v[148:151], v[116:117], off offset:256
	v_or_b32_e32 v195, 32, v181
	v_mad_i64_i32 v[116:117], s[2:3], v195, s81, v[168:169]
	global_load_dwordx4 v[144:147], v[116:117], off
	global_load_dwordx4 v[132:135], v[116:117], off offset:256
	v_and_b32_e32 v119, 64, v210
	v_xor_b32_e32 v118, 16, v210
	v_add_u32_e32 v119, 64, v119
	v_cmp_lt_i32_e32 vcc, v118, v119
	v_or_b32_e32 v194, 48, v181
	v_mad_i64_i32 v[116:117], s[2:3], v194, s81, v[168:169]
	v_cndmask_b32_e32 v118, v210, v118, vcc
	v_lshlrev_b32_e32 v180, 2, v118
	v_xor_b32_e32 v118, 32, v210
	v_cmp_lt_i32_e32 vcc, v118, v119
	v_mov_b64_e32 v[170:171], s[4:5]
	v_mad_i64_i32 v[172:173], s[2:3], v181, s81, v[170:171]
	v_cndmask_b32_e32 v118, v210, v118, vcc
	v_lshlrev_b32_e32 v179, 2, v118
	global_load_dwordx4 v[120:123], v[116:117], off
	s_nop 0
	global_load_dwordx4 v[116:119], v[116:117], off offset:256
	v_add_u32_e32 v224, 0x80, v181
	v_mad_i64_i32 v[222:223], s[4:5], v224, s81, v[168:169]
	global_load_dwordx4 v[218:221], v[222:223], off
	s_nop 0
	global_load_dwordx4 v[222:225], v[222:223], off offset:256
	v_add_u32_e32 v232, 0x90, v181
	v_mad_i64_i32 v[230:231], s[4:5], v232, s81, v[168:169]
	global_load_dwordx4 v[226:229], v[230:231], off
	s_nop 0
	global_load_dwordx4 v[230:233], v[230:231], off offset:256
	v_add_u32_e32 v240, 0xa0, v181
	v_mad_i64_i32 v[238:239], s[4:5], v240, s81, v[168:169]
	global_load_dwordx4 v[234:237], v[238:239], off
	s_nop 0
	global_load_dwordx4 v[238:241], v[238:239], off offset:256
	v_add_u32_e32 v248, 0xb0, v181
	v_mad_i64_i32 v[246:247], s[4:5], v248, s81, v[168:169]
	global_load_dwordx4 v[242:245], v[246:247], off
	s_nop 0
	global_load_dwordx4 v[246:249], v[246:247], off offset:256
	v_lshl_add_u64 v[172:173], v[172:173], 0, v[166:167]
	v_cmp_lt_i32_e32 vcc, 0, v3
	s_waitcnt vmcnt(0)
	v_lshlrev_b32_e32 v186, 16, v182
	v_and_b32_e32 v187, 0xffff0000, v182
	v_lshlrev_b32_e32 v182, 16, v183
	v_and_b32_e32 v183, 0xffff0000, v183
	v_pk_add_f32 v[142:143], v[142:143], v[182:183]
	v_lshlrev_b32_e32 v182, 16, v184
	v_and_b32_e32 v183, 0xffff0000, v184
	v_pk_add_f32 v[182:183], v[136:137], v[182:183]
	v_lshlrev_b32_e32 v136, 16, v185
	v_and_b32_e32 v137, 0xffff0000, v185
	v_pk_add_f32 v[140:141], v[140:141], v[186:187]
	v_pk_add_f32 v[184:185], v[138:139], v[136:137]
	v_cvt_pk_bf16_f32 v136, v140, v141
	v_cvt_pk_bf16_f32 v137, v142, v143
	v_cvt_pk_bf16_f32 v138, v182, v183
	v_cvt_pk_bf16_f32 v139, v184, v185
	global_store_dwordx4 v[172:173], v[136:139], off
	v_pk_mul_f32 v[190:191], v[182:183], v[182:183]
	v_pk_mul_f32 v[192:193], v[184:185], v[184:185]
	v_lshlrev_b32_e32 v136, 16, v156
	v_and_b32_e32 v137, 0xffff0000, v156
	v_pk_add_f32 v[128:129], v[128:129], v[136:137]
	v_lshlrev_b32_e32 v136, 16, v157
	v_and_b32_e32 v137, 0xffff0000, v157
	v_pk_add_f32 v[130:131], v[130:131], v[136:137]
	v_lshlrev_b32_e32 v136, 16, v158
	v_and_b32_e32 v137, 0xffff0000, v158
	v_pk_add_f32 v[136:137], v[124:125], v[136:137]
	v_lshlrev_b32_e32 v124, 16, v159
	v_and_b32_e32 v125, 0xffff0000, v159
	v_pk_add_f32 v[138:139], v[126:127], v[124:125]
	v_pk_mul_f32 v[124:125], v[128:129], v[128:129]
	v_pk_mul_f32 v[126:127], v[130:131], v[130:131]
	v_add_f32_e32 v124, v124, v125
	v_add_f32_e32 v126, v126, v127
	v_pk_mul_f32 v[186:187], v[140:141], v[140:141]
	v_pk_mul_f32 v[188:189], v[142:143], v[142:143]
	v_pk_mul_f32 v[140:141], v[136:137], v[136:137]
	v_pk_mul_f32 v[142:143], v[138:139], v[138:139]
	v_add_f32_e32 v124, v124, v126
	v_add_f32_e32 v125, v192, v193
	v_add_f32_e32 v126, v190, v191
	v_add_f32_e32 v142, v142, v143
	v_add_f32_e32 v140, v140, v141
	v_add_f32_e32 v125, v126, v125
	v_add_f32_e32 v126, v188, v189
	v_add_f32_e32 v127, v186, v187
	v_add_f32_e32 v140, v140, v142
	v_add_f32_e32 v126, v127, v126
	v_add_f32_e32 v124, v124, v140
	v_add_f32_e32 v125, v126, v125
	v_add_f32_e32 v140, v125, v124
	v_cvt_pk_bf16_f32 v124, v128, v129
	v_lshlrev_b32_e32 v128, 16, v152
	v_and_b32_e32 v129, 0xffff0000, v152
	v_pk_add_f32 v[112:113], v[112:113], v[128:129]
	v_lshlrev_b32_e32 v128, 16, v153
	v_and_b32_e32 v129, 0xffff0000, v153
	v_pk_add_f32 v[114:115], v[114:115], v[128:129]
	v_lshlrev_b32_e32 v128, 16, v154
	v_and_b32_e32 v129, 0xffff0000, v154
	v_cvt_pk_bf16_f32 v125, v130, v131
	v_cvt_pk_bf16_f32 v126, v136, v137
	v_cvt_pk_bf16_f32 v127, v138, v139
	v_pk_add_f32 v[128:129], v[108:109], v[128:129]
	v_lshlrev_b32_e32 v108, 16, v155
	v_and_b32_e32 v109, 0xffff0000, v155
	global_store_dwordx4 v[172:173], v[124:127], off offset:256
	v_pk_add_f32 v[130:131], v[110:111], v[108:109]
	v_cvt_pk_bf16_f32 v108, v112, v113
	v_mad_i64_i32 v[126:127], s[2:3], v196, s81, v[170:171]
	v_lshl_add_u64 v[126:127], v[126:127], 0, v[166:167]
	v_cvt_pk_bf16_f32 v109, v114, v115
	v_cvt_pk_bf16_f32 v110, v128, v129
	v_cvt_pk_bf16_f32 v111, v130, v131
	ds_bpermute_b32 v124, v180, v140
	global_store_dwordx4 v[126:127], v[108:111], off
	v_pk_mul_f32 v[142:143], v[130:131], v[130:131]
	v_pk_mul_f32 v[136:137], v[112:113], v[112:113]
	v_lshlrev_b32_e32 v108, 16, v148
	v_and_b32_e32 v109, 0xffff0000, v148
	v_pk_add_f32 v[104:105], v[104:105], v[108:109]
	v_lshlrev_b32_e32 v108, 16, v149
	v_and_b32_e32 v109, 0xffff0000, v149
	v_pk_add_f32 v[106:107], v[106:107], v[108:109]
	v_lshlrev_b32_e32 v108, 16, v150
	v_and_b32_e32 v109, 0xffff0000, v150
	v_pk_add_f32 v[108:109], v[100:101], v[108:109]
	v_lshlrev_b32_e32 v100, 16, v151
	v_and_b32_e32 v101, 0xffff0000, v151
	v_pk_add_f32 v[110:111], v[102:103], v[100:101]
	v_pk_mul_f32 v[100:101], v[104:105], v[104:105]
	v_pk_mul_f32 v[102:103], v[106:107], v[106:107]
	s_waitcnt lgkmcnt(0)
; __device__ __forceinline__ unsigned cvt_pk_bf16(float lo, float hi) { f32x2_c v = {lo, hi}; bf16x2_c b = __builtin_convertvector(v, bf16x2_c); return __builtin_bit_cast(unsigned, b); }
; __device__ __forceinline__ float bf_lo(unsigned u) { return __uint_as_float(u << 16); }
; __device__ __forceinline__ float bf_hi(unsigned u) { return __uint_as_float(u & 0xffff0000u); }
;     __device__ __forceinline__ void operator()(const f32x4 (&acc)[2][2][4][2], const Unit& u, int wr, int wc, int fr, int fq) const {
;     ...
;             for (int m = 0; m < 4; ++m) { const int row = row0 + ai * HALF + m * 16; bf16_t* hp = Hx + (size_t)row * LDT + col0;
;                 float ss = 0.f;
; #pragma unroll
;                 for (int bj = 0; bj < 2; ++bj) { const u32x4 x = xv[m][bj]; const f32x4 a0 = acc[ai][bj][m][0], a1 = acc[ai][bj][m][1];
;                     const float y0 = bf_lo(x.x) + a0[0] * scale, y1 = bf_hi(x.x) + a0[1] * scale, y2 = bf_lo(x.y) + a0[2] * scale, y3 = bf_hi(x.y) + a0[3] * scale;
;                     const float y4 = bf_lo(x.z) + a1[0] * scale, y5 = bf_hi(x.z) + a1[1] * scale, y6 = bf_lo(x.w) + a1[2] * scale, y7 = bf_hi(x.w) + a1[3] * scale;
;                     ss += ((y0 * y0 + y1 * y1) + (y2 * y2 + y3 * y3)) + ((y4 * y4 + y5 * y5) + (y6 * y6 + y7 * y7));
;                     u32x4 w; w.x = cvt_pk_bf16(y0, y1); w.y = cvt_pk_bf16(y2, y3); w.z = cvt_pk_bf16(y4, y5); w.w = cvt_pk_bf16(y6, y7);
;                     *(u32x4*)(hp + bj * HALF) = w; }
;                 ss += __shfl_xor(ss, 16); ss += __shfl_xor(ss, 32); ssm[m] = ss; }
;             { const float sv = (fq == 0) ? ssm[0] : (fq == 1) ? ssm[1] : (fq == 2) ? ssm[2] : ssm[3];
	v_add_f32_e32 v124, v140, v124
	v_pk_mul_f32 v[140:141], v[128:129], v[128:129]
	v_add_f32_e32 v102, v102, v103
	v_add_f32_e32 v100, v100, v101
	v_pk_mul_f32 v[138:139], v[114:115], v[114:115]
	v_pk_mul_f32 v[112:113], v[108:109], v[108:109]
	v_pk_mul_f32 v[114:115], v[110:111], v[110:111]
	v_add_f32_e32 v100, v100, v102
	v_add_f32_e32 v101, v142, v143
	v_add_f32_e32 v102, v140, v141
	v_add_f32_e32 v114, v114, v115
	v_add_f32_e32 v112, v112, v113
	v_add_f32_e32 v101, v102, v101
	v_add_f32_e32 v102, v138, v139
	v_add_f32_e32 v103, v136, v137
	v_add_f32_e32 v112, v112, v114
	v_add_f32_e32 v102, v103, v102
	v_add_f32_e32 v100, v100, v112
	v_add_f32_e32 v101, v102, v101
	v_add_f32_e32 v112, v101, v100
	v_cvt_pk_bf16_f32 v100, v104, v105
	v_lshlrev_b32_e32 v104, 16, v144
	v_and_b32_e32 v105, 0xffff0000, v144
	v_pk_add_f32 v[96:97], v[96:97], v[104:105]
	v_lshlrev_b32_e32 v104, 16, v145
	v_and_b32_e32 v105, 0xffff0000, v145
	v_pk_add_f32 v[98:99], v[98:99], v[104:105]
	v_lshlrev_b32_e32 v104, 16, v146
	v_and_b32_e32 v105, 0xffff0000, v146
	v_cvt_pk_bf16_f32 v101, v106, v107
	v_cvt_pk_bf16_f32 v102, v108, v109
	v_cvt_pk_bf16_f32 v103, v110, v111
	v_pk_add_f32 v[104:105], v[92:93], v[104:105]
	v_lshlrev_b32_e32 v92, 16, v147
	v_and_b32_e32 v93, 0xffff0000, v147
	global_store_dwordx4 v[126:127], v[100:103], off offset:256
	v_pk_add_f32 v[106:107], v[94:95], v[92:93]
	v_cvt_pk_bf16_f32 v92, v96, v97
	v_mad_i64_i32 v[102:103], s[2:3], v195, s81, v[170:171]
	v_lshl_add_u64 v[102:103], v[102:103], 0, v[166:167]
	v_cvt_pk_bf16_f32 v93, v98, v99
	v_cvt_pk_bf16_f32 v94, v104, v105
	v_cvt_pk_bf16_f32 v95, v106, v107
	ds_bpermute_b32 v100, v180, v112
	global_store_dwordx4 v[102:103], v[92:95], off
	v_pk_mul_f32 v[114:115], v[106:107], v[106:107]
	v_pk_mul_f32 v[108:109], v[96:97], v[96:97]
	v_lshlrev_b32_e32 v92, 16, v132
	v_and_b32_e32 v93, 0xffff0000, v132
	v_pk_add_f32 v[88:89], v[88:89], v[92:93]
	v_lshlrev_b32_e32 v92, 16, v133
	v_and_b32_e32 v93, 0xffff0000, v133
	v_pk_add_f32 v[90:91], v[90:91], v[92:93]
	v_lshlrev_b32_e32 v92, 16, v134
	v_and_b32_e32 v93, 0xffff0000, v134
	v_pk_add_f32 v[92:93], v[84:85], v[92:93]
	v_lshlrev_b32_e32 v84, 16, v135
	v_and_b32_e32 v85, 0xffff0000, v135
	v_pk_add_f32 v[94:95], v[86:87], v[84:85]
	v_pk_mul_f32 v[84:85], v[88:89], v[88:89]
	v_pk_mul_f32 v[86:87], v[90:91], v[90:91]
	s_waitcnt lgkmcnt(0)
	v_add_f32_e32 v100, v112, v100
	v_pk_mul_f32 v[112:113], v[104:105], v[104:105]
	v_add_f32_e32 v86, v86, v87
	v_add_f32_e32 v84, v84, v85
	v_pk_mul_f32 v[110:111], v[98:99], v[98:99]
	v_pk_mul_f32 v[96:97], v[92:93], v[92:93]
	v_pk_mul_f32 v[98:99], v[94:95], v[94:95]
	v_add_f32_e32 v84, v84, v86
	v_add_f32_e32 v85, v114, v115
	v_add_f32_e32 v86, v112, v113
	v_add_f32_e32 v98, v98, v99
	v_add_f32_e32 v96, v96, v97
	v_add_f32_e32 v85, v86, v85
	v_add_f32_e32 v86, v110, v111
	v_add_f32_e32 v87, v108, v109
	v_add_f32_e32 v96, v96, v98
	v_add_f32_e32 v86, v87, v86
	v_add_f32_e32 v84, v84, v96
	v_add_f32_e32 v85, v86, v85
	v_add_f32_e32 v96, v85, v84
	v_cvt_pk_bf16_f32 v84, v88, v89
	v_lshlrev_b32_e32 v88, 16, v120
	v_and_b32_e32 v89, 0xffff0000, v120
	v_pk_add_f32 v[80:81], v[80:81], v[88:89]
	v_lshlrev_b32_e32 v88, 16, v121
	v_and_b32_e32 v89, 0xffff0000, v121
	v_pk_add_f32 v[82:83], v[82:83], v[88:89]
	v_lshlrev_b32_e32 v88, 16, v122
	v_and_b32_e32 v89, 0xffff0000, v122
	v_cvt_pk_bf16_f32 v85, v90, v91
	v_cvt_pk_bf16_f32 v86, v92, v93
	v_cvt_pk_bf16_f32 v87, v94, v95
	v_pk_add_f32 v[88:89], v[76:77], v[88:89]
	v_lshlrev_b32_e32 v76, 16, v123
	v_and_b32_e32 v77, 0xffff0000, v123
	global_store_dwordx4 v[102:103], v[84:87], off offset:256
	v_pk_add_f32 v[90:91], v[78:79], v[76:77]
	v_cvt_pk_bf16_f32 v76, v80, v81
	v_mad_i64_i32 v[86:87], s[2:3], v194, s81, v[170:171]
	v_lshl_add_u64 v[86:87], v[86:87], 0, v[166:167]
	v_cvt_pk_bf16_f32 v77, v82, v83
	v_cvt_pk_bf16_f32 v78, v88, v89
	v_cvt_pk_bf16_f32 v79, v90, v91
	ds_bpermute_b32 v84, v180, v96
	global_store_dwordx4 v[86:87], v[76:79], off
	v_pk_mul_f32 v[98:99], v[90:91], v[90:91]
	v_pk_mul_f32 v[92:93], v[80:81], v[80:81]
	v_lshlrev_b32_e32 v76, 16, v116
	v_and_b32_e32 v77, 0xffff0000, v116
	v_pk_add_f32 v[72:73], v[72:73], v[76:77]
	v_lshlrev_b32_e32 v76, 16, v117
	v_and_b32_e32 v77, 0xffff0000, v117
	v_pk_add_f32 v[74:75], v[74:75], v[76:77]
	v_lshlrev_b32_e32 v76, 16, v118
	v_and_b32_e32 v77, 0xffff0000, v118
	v_pk_add_f32 v[76:77], v[68:69], v[76:77]
	v_lshlrev_b32_e32 v68, 16, v119
	v_and_b32_e32 v69, 0xffff0000, v119
	v_pk_add_f32 v[78:79], v[70:71], v[68:69]
	v_pk_mul_f32 v[68:69], v[72:73], v[72:73]
	v_pk_mul_f32 v[70:71], v[74:75], v[74:75]
	s_waitcnt lgkmcnt(0)
	v_add_f32_e32 v84, v96, v84
	v_pk_mul_f32 v[96:97], v[88:89], v[88:89]
	v_add_f32_e32 v70, v70, v71
	v_add_f32_e32 v68, v68, v69
	v_pk_mul_f32 v[94:95], v[82:83], v[82:83]
	v_pk_mul_f32 v[80:81], v[76:77], v[76:77]
	v_pk_mul_f32 v[82:83], v[78:79], v[78:79]
	v_add_f32_e32 v68, v68, v70
	v_add_f32_e32 v69, v98, v99
	v_add_f32_e32 v70, v96, v97
	v_add_f32_e32 v82, v82, v83
	v_add_f32_e32 v80, v80, v81
	v_add_f32_e32 v69, v70, v69
	v_add_f32_e32 v70, v94, v95
	v_add_f32_e32 v71, v92, v93
	v_add_f32_e32 v80, v80, v82
	v_add_f32_e32 v70, v71, v70
	v_add_f32_e32 v68, v68, v80
	v_add_f32_e32 v69, v70, v69
	v_add_f32_e32 v80, v69, v68
	v_cvt_pk_bf16_f32 v68, v72, v73
	v_cvt_pk_bf16_f32 v69, v74, v75
	v_cvt_pk_bf16_f32 v70, v76, v77
	v_cvt_pk_bf16_f32 v71, v78, v79
	global_store_dwordx4 v[86:87], v[68:71], off offset:256
	ds_bpermute_b32 v68, v180, v80
	ds_bpermute_b32 v125, v179, v124
	ds_bpermute_b32 v101, v179, v100
	ds_bpermute_b32 v85, v179, v84
	s_waitcnt lgkmcnt(3)
	v_add_f32_e32 v69, v80, v68
	ds_bpermute_b32 v70, v179, v69
	s_and_saveexec_b64 s[2:3], vcc
	s_xor_b64 s[4:5], exec, s[2:3]
	s_cbranch_execz .LBB0_709
	v_cmp_ne_u32_e32 vcc, 1, v3
	s_and_saveexec_b64 s[2:3], vcc
	s_xor_b64 s[10:11], exec, s[2:3]
	s_cbranch_execz .LBB0_706
	s_waitcnt lgkmcnt(0)
	v_add_f32_e32 v68, v69, v70
	v_add_f32_e32 v69, v84, v85
	v_cndmask_b32_e64 v68, v68, v69, s[6:7]

; __device__ __forceinline__ unsigned cvt_pk_bf16(float lo, float hi) { f32x2_c v = {lo, hi}; bf16x2_c b = __builtin_convertvector(v, bf16x2_c); return __builtin_bit_cast(unsigned, b); }
; __device__ __forceinline__ float bf_lo(unsigned u) { return __uint_as_float(u << 16); }
; __device__ __forceinline__ float bf_hi(unsigned u) { return __uint_as_float(u & 0xffff0000u); }
;     __device__ __forceinline__ void operator()(const f32x4 (&acc)[2][2][4][2], const Unit& u, int wr, int wc, int fr, int fq) const {
;     ...
;                 for (int bj = 0; bj < 2; ++bj) xv[m][bj] = *(const u32x4*)(Hx + (size_t)(row0 + ai * HALF + m * 16) * LDT + col0 + bj * HALF);
;             float ssm[4];
; #pragma unroll
;             for (int m = 0; m < 4; ++m) { const int row = row0 + ai * HALF + m * 16; bf16_t* hp = Hx + (size_t)row * LDT + col0;
;                 float ss = 0.f;
; #pragma unroll
;                 for (int bj = 0; bj < 2; ++bj) { const u32x4 x = xv[m][bj]; const f32x4 a0 = acc[ai][bj][m][0], a1 = acc[ai][bj][m][1];
;                     const float y0 = bf_lo(x.x) + a0[0] * scale, y1 = bf_hi(x.x) + a0[1] * scale, y2 = bf_lo(x.y) + a0[2] * scale, y3 = bf_hi(x.y) + a0[3] * scale;
;                     const float y4 = bf_lo(x.z) + a1[0] * scale, y5 = bf_hi(x.z) + a1[1] * scale, y6 = bf_lo(x.w) + a1[2] * scale, y7 = bf_hi(x.w) + a1[3] * scale;
;                     ss += ((y0 * y0 + y1 * y1) + (y2 * y2 + y3 * y3)) + ((y4 * y4 + y5 * y5) + (y6 * y6 + y7 * y7));
;                     u32x4 w; w.x = cvt_pk_bf16(y0, y1); w.y = cvt_pk_bf16(y2, y3); w.z = cvt_pk_bf16(y4, y5); w.w = cvt_pk_bf16(y6, y7);
;                     *(u32x4*)(hp + bj * HALF) = w; }
;                 ss += __shfl_xor(ss, 16); ss += __shfl_xor(ss, 32); ssm[m] = ss; }
;             { const float sv = (fq == 0) ? ssm[0] : (fq == 1) ? ssm[1] : (fq == 2) ? ssm[2] : ssm[3];
;               ssq[(size_t)(row0 + ai * HALF + fq * 16) * 32 + u.pn * 4 + wc] = sv; }
.LBB0_711:
	s_or_b64 exec, exec, s[4:5]
	v_or_b32_e32 v92, v181, v175
	v_ashrrev_i32_e32 v93, 31, v92
	s_lshl_b32 s10, s0, 2
	s_waitcnt lgkmcnt(0)
	v_lshlrev_b64 v[70:71], 7, v[92:93]
	s_ashr_i32 s11, s10, 31
	v_lshl_add_u64 v[70:71], s[14:15], 0, v[70:71]
	v_lshl_add_u64 v[70:71], s[10:11], 2, v[70:71]
	s_lshl_b32 s0, s35, 2
	v_lshl_add_u64 v[70:71], v[70:71], 0, s[0:1]
	global_store_dword v[70:71], v68, off
	v_add_u32_e32 v97, 0x80, v181
	v_mad_i64_i32 v[68:69], s[2:3], v97, s81, v[168:169]
	v_add_u32_e32 v116, 0x90, v181
	v_mad_i64_i32 v[68:69], s[2:3], v116, s81, v[168:169]
	v_add_u32_e32 v96, 0xa0, v181
	v_mad_i64_i32 v[68:69], s[2:3], v96, s81, v[168:169]
	v_add_u32_e32 v93, 0xb0, v181
	v_mad_i64_i32 v[68:69], s[2:3], v93, s81, v[168:169]
	s_nop 0
	v_readlane_b32 s2, v254, 23
	v_readlane_b32 s3, v254, 24
	v_cmp_lt_i32_e32 vcc, 0, v3
	v_lshlrev_b32_e32 v108, 16, v218
	v_and_b32_e32 v109, 0xffff0000, v218
	v_lshlrev_b32_e32 v98, 16, v219
	v_and_b32_e32 v99, 0xffff0000, v219
	v_pk_add_f32 v[58:59], v[58:59], v[98:99]
	v_lshlrev_b32_e32 v98, 16, v220
	v_and_b32_e32 v99, 0xffff0000, v220
	v_mov_b64_e32 v[94:95], s[2:3]
	v_pk_add_f32 v[98:99], v[52:53], v[98:99]
	v_lshlrev_b32_e32 v52, 16, v221
	v_and_b32_e32 v53, 0xffff0000, v221
	v_mad_i64_i32 v[106:107], s[2:3], v97, s81, v[94:95]
	v_pk_add_f32 v[56:57], v[56:57], v[108:109]
	v_pk_add_f32 v[100:101], v[54:55], v[52:53]
	v_lshl_add_u64 v[106:107], v[106:107], 0, v[166:167]
	v_cvt_pk_bf16_f32 v52, v56, v57
	v_cvt_pk_bf16_f32 v53, v58, v59
	v_cvt_pk_bf16_f32 v54, v98, v99
	v_cvt_pk_bf16_f32 v55, v100, v101
	global_store_dwordx4 v[106:107], v[52:55], off
	v_pk_mul_f32 v[108:109], v[56:57], v[56:57]
	v_pk_mul_f32 v[110:111], v[58:59], v[58:59]
	v_lshlrev_b32_e32 v52, 16, v222
	v_and_b32_e32 v53, 0xffff0000, v222
	v_lshlrev_b32_e32 v54, 16, v223
	v_and_b32_e32 v55, 0xffff0000, v223
	v_pk_add_f32 v[52:53], v[64:65], v[52:53]
	v_pk_add_f32 v[54:55], v[66:67], v[54:55]
	v_lshlrev_b32_e32 v56, 16, v224
	v_and_b32_e32 v57, 0xffff0000, v224
	v_lshlrev_b32_e32 v58, 16, v225
	v_and_b32_e32 v59, 0xffff0000, v225
	v_pk_add_f32 v[56:57], v[60:61], v[56:57]
	v_pk_add_f32 v[58:59], v[62:63], v[58:59]
	v_pk_mul_f32 v[60:61], v[52:53], v[52:53]
	v_pk_mul_f32 v[62:63], v[54:55], v[54:55]
	v_pk_mul_f32 v[112:113], v[98:99], v[98:99]
	v_pk_mul_f32 v[114:115], v[100:101], v[100:101]
	v_add_f32_e32 v62, v62, v63
	v_add_f32_e32 v60, v60, v61
	v_pk_mul_f32 v[64:65], v[56:57], v[56:57]
	v_pk_mul_f32 v[66:67], v[58:59], v[58:59]
	v_add_f32_e32 v60, v60, v62
	v_add_f32_e32 v61, v114, v115
	v_add_f32_e32 v62, v112, v113
	v_add_f32_e32 v66, v66, v67
	v_add_f32_e32 v64, v64, v65
	v_add_f32_e32 v61, v62, v61
	v_add_f32_e32 v62, v110, v111
	v_add_f32_e32 v63, v108, v109
	v_add_f32_e32 v64, v64, v66
	v_add_f32_e32 v62, v63, v62
	v_add_f32_e32 v60, v60, v64
	v_add_f32_e32 v61, v62, v61
	v_add_f32_e32 v60, v61, v60
	v_cvt_pk_bf16_f32 v52, v52, v53
	v_cvt_pk_bf16_f32 v53, v54, v55
	v_cvt_pk_bf16_f32 v54, v56, v57
	v_cvt_pk_bf16_f32 v55, v58, v59
	global_store_dwordx4 v[106:107], v[52:55], off offset:256
	ds_bpermute_b32 v52, v180, v60
	v_lshlrev_b32_e32 v56, 16, v226
	v_and_b32_e32 v57, 0xffff0000, v226
	v_pk_add_f32 v[48:49], v[48:49], v[56:57]
	v_lshlrev_b32_e32 v56, 16, v227
	v_and_b32_e32 v57, 0xffff0000, v227
	v_pk_add_f32 v[50:51], v[50:51], v[56:57]
	v_lshlrev_b32_e32 v56, 16, v228
	v_and_b32_e32 v57, 0xffff0000, v228
	v_pk_add_f32 v[56:57], v[44:45], v[56:57]
	v_lshlrev_b32_e32 v44, 16, v229
	v_and_b32_e32 v45, 0xffff0000, v229
	s_waitcnt lgkmcnt(0)
	v_add_f32_e32 v54, v60, v52
	v_mad_i64_i32 v[52:53], s[2:3], v116, s81, v[94:95]
	v_pk_add_f32 v[58:59], v[46:47], v[44:45]
	v_lshl_add_u64 v[52:53], v[52:53], 0, v[166:167]
	v_cvt_pk_bf16_f32 v44, v48, v49
	v_cvt_pk_bf16_f32 v45, v50, v51
	v_cvt_pk_bf16_f32 v46, v56, v57
	v_cvt_pk_bf16_f32 v47, v58, v59
	global_store_dwordx4 v[52:53], v[44:47], off
	v_pk_mul_f32 v[64:65], v[56:57], v[56:57]
	v_pk_mul_f32 v[66:67], v[58:59], v[58:59]
	v_lshlrev_b32_e32 v44, 16, v230
	v_and_b32_e32 v45, 0xffff0000, v230
	v_pk_add_f32 v[40:41], v[40:41], v[44:45]
	v_lshlrev_b32_e32 v44, 16, v231
	v_and_b32_e32 v45, 0xffff0000, v231
	v_pk_add_f32 v[42:43], v[42:43], v[44:45]
	v_lshlrev_b32_e32 v44, 16, v232
	v_and_b32_e32 v45, 0xffff0000, v232
	v_pk_add_f32 v[44:45], v[36:37], v[44:45]
	v_lshlrev_b32_e32 v36, 16, v233
	v_and_b32_e32 v37, 0xffff0000, v233
	v_pk_add_f32 v[46:47], v[38:39], v[36:37]
	v_pk_mul_f32 v[36:37], v[40:41], v[40:41]
	v_pk_mul_f32 v[38:39], v[42:43], v[42:43]
	v_add_f32_e32 v36, v36, v37
	v_add_f32_e32 v38, v38, v39
	v_pk_mul_f32 v[60:61], v[48:49], v[48:49]
	v_pk_mul_f32 v[62:63], v[50:51], v[50:51]
	v_pk_mul_f32 v[48:49], v[44:45], v[44:45]
	v_pk_mul_f32 v[50:51], v[46:47], v[46:47]
	v_add_f32_e32 v36, v36, v38
	v_add_f32_e32 v37, v66, v67
	v_add_f32_e32 v38, v64, v65
	v_add_f32_e32 v50, v50, v51
	v_add_f32_e32 v48, v48, v49
	v_add_f32_e32 v37, v38, v37
	v_add_f32_e32 v38, v62, v63
	v_add_f32_e32 v39, v60, v61
	v_add_f32_e32 v48, v48, v50
	v_add_f32_e32 v38, v39, v38
	v_add_f32_e32 v36, v36, v48
	v_add_f32_e32 v37, v38, v37
	v_add_f32_e32 v48, v37, v36
	v_cvt_pk_bf16_f32 v36, v40, v41
	v_lshlrev_b32_e32 v40, 16, v234
	v_and_b32_e32 v41, 0xffff0000, v234
	v_pk_add_f32 v[32:33], v[32:33], v[40:41]
	v_lshlrev_b32_e32 v40, 16, v235
	v_and_b32_e32 v41, 0xffff0000, v235
	v_pk_add_f32 v[34:35], v[34:35], v[40:41]
	v_lshlrev_b32_e32 v40, 16, v236
	v_and_b32_e32 v41, 0xffff0000, v236
	v_cvt_pk_bf16_f32 v37, v42, v43
	v_cvt_pk_bf16_f32 v38, v44, v45
	v_cvt_pk_bf16_f32 v39, v46, v47
	v_pk_add_f32 v[40:41], v[28:29], v[40:41]
	v_lshlrev_b32_e32 v28, 16, v237
	v_and_b32_e32 v29, 0xffff0000, v237
	global_store_dwordx4 v[52:53], v[36:39], off offset:256
	v_pk_add_f32 v[42:43], v[30:31], v[28:29]
	v_cvt_pk_bf16_f32 v28, v32, v33
	v_mad_i64_i32 v[38:39], s[2:3], v96, s81, v[94:95]
	v_lshl_add_u64 v[38:39], v[38:39], 0, v[166:167]
	v_cvt_pk_bf16_f32 v29, v34, v35
	v_cvt_pk_bf16_f32 v30, v40, v41
	v_cvt_pk_bf16_f32 v31, v42, v43
	ds_bpermute_b32 v36, v180, v48
	global_store_dwordx4 v[38:39], v[28:31], off
	v_pk_mul_f32 v[50:51], v[42:43], v[42:43]
	v_pk_mul_f32 v[44:45], v[32:33], v[32:33]
	v_lshlrev_b32_e32 v28, 16, v238
	v_and_b32_e32 v29, 0xffff0000, v238
	v_pk_add_f32 v[24:25], v[24:25], v[28:29]
	v_lshlrev_b32_e32 v28, 16, v239
	v_and_b32_e32 v29, 0xffff0000, v239
	v_pk_add_f32 v[26:27], v[26:27], v[28:29]
	v_lshlrev_b32_e32 v28, 16, v240
	v_and_b32_e32 v29, 0xffff0000, v240
	v_pk_add_f32 v[28:29], v[20:21], v[28:29]
	v_lshlrev_b32_e32 v20, 16, v241
	v_and_b32_e32 v21, 0xffff0000, v241
	v_pk_add_f32 v[30:31], v[22:23], v[20:21]
	v_pk_mul_f32 v[20:21], v[24:25], v[24:25]
	v_pk_mul_f32 v[22:23], v[26:27], v[26:27]
	s_waitcnt lgkmcnt(0)
; __device__ __forceinline__ unsigned cvt_pk_bf16(float lo, float hi) { f32x2_c v = {lo, hi}; bf16x2_c b = __builtin_convertvector(v, bf16x2_c); return __builtin_bit_cast(unsigned, b); }
; __device__ __forceinline__ float bf_lo(unsigned u) { return __uint_as_float(u << 16); }
; __device__ __forceinline__ float bf_hi(unsigned u) { return __uint_as_float(u & 0xffff0000u); }
;     __device__ __forceinline__ void operator()(const f32x4 (&acc)[2][2][4][2], const Unit& u, int wr, int wc, int fr, int fq) const {
;     ...
;             for (int m = 0; m < 4; ++m) { const int row = row0 + ai * HALF + m * 16; bf16_t* hp = Hx + (size_t)row * LDT + col0;
;                 float ss = 0.f;
; #pragma unroll
;                 for (int bj = 0; bj < 2; ++bj) { const u32x4 x = xv[m][bj]; const f32x4 a0 = acc[ai][bj][m][0], a1 = acc[ai][bj][m][1];
;                     const float y0 = bf_lo(x.x) + a0[0] * scale, y1 = bf_hi(x.x) + a0[1] * scale, y2 = bf_lo(x.y) + a0[2] * scale, y3 = bf_hi(x.y) + a0[3] * scale;
;                     const float y4 = bf_lo(x.z) + a1[0] * scale, y5 = bf_hi(x.z) + a1[1] * scale, y6 = bf_lo(x.w) + a1[2] * scale, y7 = bf_hi(x.w) + a1[3] * scale;
;                     ss += ((y0 * y0 + y1 * y1) + (y2 * y2 + y3 * y3)) + ((y4 * y4 + y5 * y5) + (y6 * y6 + y7 * y7));
;                     u32x4 w; w.x = cvt_pk_bf16(y0, y1); w.y = cvt_pk_bf16(y2, y3); w.z = cvt_pk_bf16(y4, y5); w.w = cvt_pk_bf16(y6, y7);
;                     *(u32x4*)(hp + bj * HALF) = w; }
;                 ss += __shfl_xor(ss, 16); ss += __shfl_xor(ss, 32); ssm[m] = ss; }
;             { const float sv = (fq == 0) ? ssm[0] : (fq == 1) ? ssm[1] : (fq == 2) ? ssm[2] : ssm[3];
	v_add_f32_e32 v36, v48, v36
	v_pk_mul_f32 v[48:49], v[40:41], v[40:41]
	v_add_f32_e32 v22, v22, v23
	v_add_f32_e32 v20, v20, v21
	v_pk_mul_f32 v[46:47], v[34:35], v[34:35]
	v_pk_mul_f32 v[32:33], v[28:29], v[28:29]
	v_pk_mul_f32 v[34:35], v[30:31], v[30:31]
	v_add_f32_e32 v20, v20, v22
	v_add_f32_e32 v21, v50, v51
	v_add_f32_e32 v22, v48, v49
	v_add_f32_e32 v34, v34, v35
	v_add_f32_e32 v32, v32, v33
	v_add_f32_e32 v21, v22, v21
	v_add_f32_e32 v22, v46, v47
	v_add_f32_e32 v23, v44, v45
	v_add_f32_e32 v32, v32, v34
	v_add_f32_e32 v22, v23, v22
	v_add_f32_e32 v20, v20, v32
	v_add_f32_e32 v21, v22, v21
	v_add_f32_e32 v32, v21, v20
	v_cvt_pk_bf16_f32 v20, v24, v25
	v_lshlrev_b32_e32 v24, 16, v242
	v_and_b32_e32 v25, 0xffff0000, v242
	v_pk_add_f32 v[16:17], v[16:17], v[24:25]
	v_lshlrev_b32_e32 v24, 16, v243
	v_and_b32_e32 v25, 0xffff0000, v243
	v_pk_add_f32 v[18:19], v[18:19], v[24:25]
	v_lshlrev_b32_e32 v24, 16, v244
	v_and_b32_e32 v25, 0xffff0000, v244
	v_cvt_pk_bf16_f32 v21, v26, v27
	v_cvt_pk_bf16_f32 v22, v28, v29
	v_cvt_pk_bf16_f32 v23, v30, v31
	v_pk_add_f32 v[24:25], v[12:13], v[24:25]
	v_lshlrev_b32_e32 v12, 16, v245
	v_and_b32_e32 v13, 0xffff0000, v245
	global_store_dwordx4 v[38:39], v[20:23], off offset:256
	v_pk_add_f32 v[26:27], v[14:15], v[12:13]
	v_cvt_pk_bf16_f32 v12, v16, v17
	v_mad_i64_i32 v[22:23], s[2:3], v93, s81, v[94:95]
	v_lshl_add_u64 v[22:23], v[22:23], 0, v[166:167]
	v_cvt_pk_bf16_f32 v13, v18, v19
	v_cvt_pk_bf16_f32 v14, v24, v25
	v_cvt_pk_bf16_f32 v15, v26, v27
	ds_bpermute_b32 v20, v180, v32
	global_store_dwordx4 v[22:23], v[12:15], off
	v_pk_mul_f32 v[34:35], v[26:27], v[26:27]
	v_pk_mul_f32 v[28:29], v[16:17], v[16:17]
	v_lshlrev_b32_e32 v12, 16, v246
	v_and_b32_e32 v13, 0xffff0000, v246
	v_pk_add_f32 v[8:9], v[8:9], v[12:13]
	v_lshlrev_b32_e32 v12, 16, v247
	v_and_b32_e32 v13, 0xffff0000, v247
	v_pk_add_f32 v[10:11], v[10:11], v[12:13]
	v_lshlrev_b32_e32 v12, 16, v248
	v_and_b32_e32 v13, 0xffff0000, v248
	v_pk_add_f32 v[12:13], v[4:5], v[12:13]
	v_lshlrev_b32_e32 v4, 16, v249
	v_and_b32_e32 v5, 0xffff0000, v249
	v_pk_add_f32 v[14:15], v[6:7], v[4:5]
	v_pk_mul_f32 v[4:5], v[8:9], v[8:9]
	v_pk_mul_f32 v[6:7], v[10:11], v[10:11]
	s_waitcnt lgkmcnt(0)
	v_add_f32_e32 v20, v32, v20
	v_pk_mul_f32 v[32:33], v[24:25], v[24:25]
	v_add_f32_e32 v6, v6, v7
	v_add_f32_e32 v4, v4, v5
	v_pk_mul_f32 v[30:31], v[18:19], v[18:19]
	v_pk_mul_f32 v[16:17], v[12:13], v[12:13]
	v_pk_mul_f32 v[18:19], v[14:15], v[14:15]
	v_add_f32_e32 v4, v4, v6
	v_add_f32_e32 v5, v34, v35
	v_add_f32_e32 v6, v32, v33
	v_add_f32_e32 v18, v18, v19
	v_add_f32_e32 v16, v16, v17
	v_add_f32_e32 v5, v6, v5
	v_add_f32_e32 v6, v30, v31
	v_add_f32_e32 v7, v28, v29
	v_add_f32_e32 v16, v16, v18
	v_add_f32_e32 v6, v7, v6
	v_add_f32_e32 v4, v4, v16
	v_add_f32_e32 v5, v6, v5
	v_add_f32_e32 v16, v5, v4
	v_cvt_pk_bf16_f32 v4, v8, v9
	v_cvt_pk_bf16_f32 v5, v10, v11
	v_cvt_pk_bf16_f32 v6, v12, v13
	v_cvt_pk_bf16_f32 v7, v14, v15
	global_store_dwordx4 v[22:23], v[4:7], off offset:256
	ds_bpermute_b32 v4, v180, v16
	ds_bpermute_b32 v55, v179, v54
	ds_bpermute_b32 v37, v179, v36
	ds_bpermute_b32 v21, v179, v20
	s_waitcnt lgkmcnt(3)
	v_add_f32_e32 v5, v16, v4
	ds_bpermute_b32 v6, v179, v5
	s_and_saveexec_b64 s[2:3], vcc
	s_xor_b64 s[4:5], exec, s[2:3]
	s_cbranch_execz .LBB0_717
	v_cmp_ne_u32_e32 vcc, 1, v3
	s_and_saveexec_b64 s[2:3], vcc
	s_xor_b64 s[24:25], exec, s[2:3]
	s_cbranch_execz .LBB0_714
	s_waitcnt lgkmcnt(0)
	v_add_f32_e32 v4, v5, v6
	v_add_f32_e32 v5, v20, v21
	v_cndmask_b32_e64 v4, v4, v5, s[6:7]
